# static priority raise (s_setprio 3) for the K1 scan waves over the MFMA GEMM waves sharing their SIMDs; otherwise identical to the ring-16 hybrid
# baseline (speedup 1.0000x reference)
.Lk1_scan:
	s_setprio 3
	s_load_dwordx2 s[4:5], s[0:1], 0x0
	s_load_dwordx4 s[8:11], s[0:1], 0x20
	s_load_dwordx2 s[12:13], s[0:1], 0x30
	v_and_b32_e32 v6, 63, v0
	v_readfirstlane_b32 s3, v0
	v_lshlrev_b32_e32 v1, 4, v6
	v_lshlrev_b32_e32 v2, 2, v6
	v_or_b32_e32 v3, 1, v2
	v_or_b32_e32 v4, 2, v2
	v_or_b32_e32 v5, 3, v2
	s_lshr_b32 s3, s3, 6
	s_sub_u32 s16, s2, 0x60
	s_lshl_b32 s16, s16, 2
	s_add_u32 s16, s16, s3
	s_mul_i32 s17, s16, 0x48000
	s_lshr_b32 s18, s17, 2
	s_lshl_b32 s24, s3, 13
	s_mov_b32 s25, s24
	s_mov_b32 s28, s24
	s_mov_b32 s36, 0
	s_mov_b64 s[62:63], 0
	v_mov_b32_e32 v21, 1
	s_mov_b32 s27, 0
	s_mov_b32 s29, 0x55555556
	s_mov_b32 s31, 0xc0000
	s_waitcnt lgkmcnt(0)
	s_and_b32 s50, s16, 15
	s_mul_i32 s52, s50, 512
	s_add_u32 s52, s52, 28672
	s_lshl_b32 s53, s50, 6
	s_add_u32 s53, s53, 0xe000
	s_add_u32 s54, s10, s53
	s_addc_u32 s55, s11, 0
	s_mul_i32 s59, s16, 14
	s_mul_i32 s57, s59, 0x4000
	s_lshr_b32 s18, s57, 2
	s_add_u32 s6, s4, s57
	s_addc_u32 s7, s5, 0
	v_mov_b32_e32 v27, 0
	global_load_dwordx4 v[28:31], v1, s[6:7] nt
	s_add_u32 s6, s6, 0x400
	s_addc_u32 s7, s7, 0
	global_load_dwordx4 v[32:35], v1, s[6:7] nt
	s_add_u32 s6, s6, 0x400
	s_addc_u32 s7, s7, 0
	global_load_dwordx4 v[36:39], v1, s[6:7] nt
	s_add_u32 s6, s6, 0x400
	s_addc_u32 s7, s7, 0
	global_load_dwordx4 v[40:43], v1, s[6:7] nt
	s_add_u32 s6, s6, 0x400
	s_addc_u32 s7, s7, 0
	global_load_dwordx4 v[44:47], v1, s[6:7] nt
	s_add_u32 s6, s6, 0x400
	s_addc_u32 s7, s7, 0
	global_load_dwordx4 v[48:51], v1, s[6:7] nt
	s_add_u32 s6, s6, 0x400
	s_addc_u32 s7, s7, 0
	global_load_dwordx4 v[52:55], v1, s[6:7] nt
	s_add_u32 s6, s6, 0x400
	s_addc_u32 s7, s7, 0
	global_load_dwordx4 v[56:59], v1, s[6:7] nt
	s_add_u32 s6, s6, 0x400
	s_addc_u32 s7, s7, 0
	global_load_dwordx4 v[60:63], v1, s[6:7] nt
	s_add_u32 s6, s6, 0x400
	s_addc_u32 s7, s7, 0
	global_load_dwordx4 v[64:67], v1, s[6:7] nt
	s_add_u32 s6, s6, 0x400
	s_addc_u32 s7, s7, 0
	global_load_dwordx4 v[68:71], v1, s[6:7] nt
	s_add_u32 s6, s6, 0x400
	s_addc_u32 s7, s7, 0
	global_load_dwordx4 v[72:75], v1, s[6:7] nt
	s_add_u32 s6, s6, 0x400
	s_addc_u32 s7, s7, 0
	global_load_dwordx4 v[76:79], v1, s[6:7] nt
	s_add_u32 s6, s6, 0x400
	s_addc_u32 s7, s7, 0
	global_load_dwordx4 v[80:83], v1, s[6:7] nt
	s_add_u32 s6, s6, 0x400
	s_addc_u32 s7, s7, 0
	global_load_dwordx4 v[84:87], v1, s[6:7] nt
	s_add_u32 s6, s6, 0x400
	s_addc_u32 s7, s7, 0
	global_load_dwordx4 v[88:91], v1, s[6:7] nt
	s_add_u32 s6, s6, 0x400
	s_addc_u32 s7, s7, 0
	s_mov_b32 s26, 18
	s_add_u32 s57, s59, 1
	s_mul_i32 s57, s57, 0x4000
	s_lshr_b32 s58, s57, 2
	s_add_u32 s6, s4, s57
	s_addc_u32 s7, s5, 0
	s_mov_b32 s26, 0
